# peersel last stage: the second half-workgroup runs it on its waves 2,3 (the first half on 0,1), so the two halves no longer share SIMDs 0,1 for that stage
# speedup vs baseline: 1.0093x; 1.0043x over previous
; DI int tidx() { int t = threadIdx.x & 255; asm volatile("" : "+v"(t)); return t; }
; DI void peer_select_unit(const Params& p, int unit, char* lds, const bf16x8 (&kb)[4][4]) {
;     ...
;     const int set = wid >> 1, kh = wid & 1;
;     bf16x8 qa[2][4];
; #pragma unroll
;     for (int mt = 0; mt < 2; ++mt)
; #pragma unroll
;       for (int kk = 0; kk < 4; ++kk) qa[mt][kk] = *(const bf16x8*)(qy + (size_t)(t0 + 16 * mt + fr) * 2048 + h * 256 + set * 128 + kk * 32 + fq * 8);
; DI void phase_peersel(const Params& p, int bid, int nb, char* lds) {
;   const int lane = tidx() & 63, wid = tidx() >> 6, fr = lane & 15, fq = lane >> 4;
;   const bf16_t* keys = (const bf16_t*)(p.ws + WS_KEYS) + (wid >> 1) * 16384 + (wid & 1) * 64 * 128;
;   bf16x8 kb[4][4];
; #pragma unroll
;   for (int nj = 0; nj < 4; ++nj)
; #pragma unroll
;     for (int kk = 0; kk < 4; ++kk) kb[nj][kk] = *(const bf16x8*)(keys + (16 * nj + fr) * 128 + kk * 32 + fq * 8);
;   for (int u = bid; u < 8192; u += nb) peer_select_unit(p, u, lds, kb);
.LBB0_1648:
	s_or_b64 exec, exec, s[0:1]
	v_lshrrev_b32_e32 v249, 8, v207
	v_lshlrev_b32_e32 v249, 7, v249
	v_and_b32_e32 v248, 3, v206
	v_lshlrev_b32_e32 v248, 4, v248
	s_getpc_b64 s[0:1]
	s_add_u32 s0, s0, _ZL9PEER_CAND@rel32@lo+4
	s_addc_u32 s1, s1, _ZL9PEER_CAND@rel32@hi+12
	global_load_dwordx4 v[244:247], v248, s[0:1]
	s_waitcnt vmcnt(0)
	s_movk_i32 s0, 0x2000
	s_waitcnt lgkmcnt(0)
	v_mov_b32_e32 v0, v206
	v_mov_b32_e32 v1, v206
	v_cmp_gt_i32_e32 vcc, s0, v176
	s_barrier
	s_and_saveexec_b64 s[52:53], vcc
	s_cbranch_execz .LBB0_1683
	v_lshlrev_b32_e32 v2, 7, v1
	v_and_b32_e32 v2, 0xffffc000, v2
	v_readlane_b32 s2, v250, 7
	v_ashrrev_i32_e32 v3, 31, v2
	v_readlane_b32 s3, v250, 8
	v_lshlrev_b32_e32 v1, 8, v1
	v_and_b32_e32 v64, 0x4000, v1
	v_lshl_add_u64 v[2:3], v[2:3], 1, s[2:3]
	v_mov_b32_e32 v65, 0
	v_lshl_add_u64 v[2:3], v[2:3], 0, v[64:65]
	v_and_b32_e32 v64, 48, v0
	v_lshlrev_b32_e32 v0, 8, v0
	v_lshl_add_u64 v[2:3], v[2:3], 0, v[64:65]
	v_and_b32_e32 v64, 0xf00, v0
	v_lshl_add_u64 v[40:41], v[2:3], 0, v[64:65]
	s_movk_i32 s1, 0x1000
	v_add_co_u32_e32 v66, vcc, s1, v40
	global_load_dwordx4 v[0:3], v[40:41], off
	global_load_dwordx4 v[4:7], v[40:41], off offset:64
	global_load_dwordx4 v[8:11], v[40:41], off offset:128
	global_load_dwordx4 v[12:15], v[40:41], off offset:192
	v_addc_co_u32_e32 v67, vcc, 0, v41, vcc
	v_add_co_u32_e32 v68, vcc, s0, v40
	s_movk_i32 s0, 0x3000
	s_nop 0
	v_addc_co_u32_e32 v69, vcc, 0, v41, vcc
	v_add_co_u32_e32 v70, vcc, s0, v40
	global_load_dwordx4 v[16:19], v[66:67], off offset:64
	global_load_dwordx4 v[20:23], v[66:67], off offset:128
	global_load_dwordx4 v[24:27], v[68:69], off
	global_load_dwordx4 v[28:31], v[68:69], off offset:64
	global_load_dwordx4 v[32:35], v[68:69], off offset:128
	global_load_dwordx4 v[36:39], v[68:69], off offset:192
	v_addc_co_u32_e32 v71, vcc, 0, v41, vcc
	global_load_dwordx4 v[40:43], v[66:67], off offset:192
	global_load_dwordx4 v[44:47], v[70:71], off
	global_load_dwordx4 v[48:51], v[70:71], off offset:64
	global_load_dwordx4 v[52:55], v[70:71], off offset:128
	global_load_dwordx4 v[56:59], v[68:69], off offset:-4096
	global_load_dwordx4 v[60:63], v[70:71], off offset:192
	s_add_u32 s60, s84, 0x12000000
	s_addc_u32 s61, s85, 0
	s_add_u32 s62, s84, 0x13000000
	s_addc_u32 s63, s85, 0
	s_mov_b64 s[64:65], 0
	s_movk_i32 s2, 0x210
	s_movk_i32 s3, 0x7f
	s_movk_i32 s18, 0x80
	s_movk_i32 s19, 0xff
	s_movk_i32 s68, 0x1fff
	v_mov_b32_e32 v72, v176
	v_and_b32_e32 v182, 15, v206
	v_lshlrev_b32_e32 v182, 12, v182
	v_bfe_u32 v183, v206, 4, 2
	v_lshl_or_b32 v182, v183, 4, v182
	v_lshrrev_b32_e32 v183, 7, v206
	v_lshl_or_b32 v182, v183, 8, v182
	v_mov_b32_e32 v183, 0
	v_lshl_add_u64 v[182:183], s[58:59], 0, v[182:183]
	v_mov_b32_e32 v184, v72
	v_lshrrev_b32_e32 v185, 3, v184
	v_lshlrev_b32_e32 v185, 17, v185
	v_and_b32_e32 v184, 7, v184
	v_lshl_or_b32 v184, v184, 9, v185
	v_mov_b32_e32 v185, 0
	v_lshl_add_u64 v[184:185], v[182:183], 0, v[184:185]
	v_mov_b32_e32 v186, 0x10000
	v_mov_b32_e32 v187, 0
	v_lshl_add_u64 v[186:187], v[184:185], 0, v[186:187]
	global_load_dwordx4 v[148:151], v[184:185], off
	global_load_dwordx4 v[152:155], v[184:185], off offset:64
	global_load_dwordx4 v[156:159], v[186:187], off
	global_load_dwordx4 v[160:163], v[186:187], off offset:64
	global_load_dwordx4 v[164:167], v[184:185], off offset:128
	global_load_dwordx4 v[168:171], v[184:185], off offset:192
	global_load_dwordx4 v[172:175], v[186:187], off offset:128
	global_load_dwordx4 v[178:181], v[186:187], off offset:192
	s_branch .LBB0_1652

; DI unsigned ordkey(float f) { const unsigned u = __float_as_uint(f); return (u & 0x80000000u) ? ~u : (u | 0x80000000u); }
; DI void peer_select_unit(const Params& p, int unit, char* lds, const bf16x8 (&kb)[4][4]) {
;     ...
;   for (int pass = 0; pass < 2; ++pass) {
;     const int rr = pass * 32 + (tid >> 3), part = tid & 7;
;     unsigned a[16], bq[16];
;     const float* srow = sc + rr * 132 + 16 * part;
; #pragma unroll
;     for (int j = 0; j < 4; ++j) {
;       const f32x4 v = *(const f32x4*)(srow + 4 * j);
; #pragma unroll
;       for (int e = 0; e < 4; ++e) a[4 * j + e] = (ordkey(v[e]) & ~127u) | (unsigned)(127 - (16 * part + 4 * j + e));
;     }
;     sort16_desc(a);
.LBB0_1653:
	v_add_u32_e32 v71, s69, v64
	v_mul_lo_u32 v76, v71, s2
	v_add_u32_e32 v77, v68, v76
	ds_read_b128 v[78:81], v77
	ds_read_b128 v[82:85], v77 offset:16
	ds_read_b128 v[86:89], v77 offset:32
	ds_read_b128 v[90:93], v77 offset:48
	v_cndmask_b32_e64 v70, 0, 1, s[20:21]
	s_waitcnt lgkmcnt(3)
	v_not_b32_e32 v77, v78
	v_or_b32_e32 v94, 0x80000000, v78
	v_not_b32_e32 v95, v79
	v_or_b32_e32 v96, 0x80000000, v79
	v_cmp_gt_i32_e32 vcc, 0, v79
	v_not_b32_e32 v79, v80
	v_or_b32_e32 v97, 0x80000000, v80
	v_cmp_gt_i32_e64 s[20:21], 0, v80
	v_not_b32_e32 v80, v81
	v_or_b32_e32 v98, 0x80000000, v81
	v_cmp_gt_i32_e64 s[22:23], 0, v81
	s_waitcnt lgkmcnt(2)
	v_not_b32_e32 v81, v82
	v_or_b32_e32 v99, 0x80000000, v82
	v_cmp_gt_i32_e64 s[24:25], 0, v82
	v_not_b32_e32 v82, v83
	v_or_b32_e32 v100, 0x80000000, v83
	v_cmp_gt_i32_e64 s[26:27], 0, v83
	v_not_b32_e32 v83, v84
	v_or_b32_e32 v101, 0x80000000, v84
	v_cmp_gt_i32_e64 s[28:29], 0, v84
	v_not_b32_e32 v84, v85
	v_or_b32_e32 v102, 0x80000000, v85
	v_cmp_gt_i32_e64 s[30:31], 0, v85
	s_waitcnt lgkmcnt(1)
	v_not_b32_e32 v85, v86
	v_or_b32_e32 v103, 0x80000000, v86
	v_cmp_gt_i32_e64 s[34:35], 0, v86
	v_not_b32_e32 v86, v87
	v_or_b32_e32 v104, 0x80000000, v87
	v_cmp_gt_i32_e64 s[36:37], 0, v87
	v_not_b32_e32 v87, v88
	v_or_b32_e32 v105, 0x80000000, v88
	v_cmp_gt_i32_e64 s[38:39], 0, v88
	v_not_b32_e32 v88, v89
	v_or_b32_e32 v106, 0x80000000, v89
	v_cmp_gt_i32_e64 s[40:41], 0, v89
	s_waitcnt lgkmcnt(0)
	v_not_b32_e32 v89, v90
	v_or_b32_e32 v107, 0x80000000, v90
	v_cmp_gt_i32_e64 s[42:43], 0, v90
	v_not_b32_e32 v90, v91
	v_or_b32_e32 v108, 0x80000000, v91
	v_cmp_gt_i32_e64 s[44:45], 0, v91
	v_not_b32_e32 v91, v92
	v_or_b32_e32 v109, 0x80000000, v92
	v_cmp_gt_i32_e64 s[46:47], 0, v92
	v_not_b32_e32 v92, v93
	v_or_b32_e32 v110, 0x80000000, v93
	v_cmp_gt_i32_e64 s[48:49], 0, v93
	v_cmp_gt_i32_e64 s[50:51], 0, v78
	v_cndmask_b32_e32 v78, v96, v95, vcc
	v_cndmask_b32_e64 v79, v97, v79, s[20:21]
	v_cndmask_b32_e64 v77, v94, v77, s[50:51]
	v_cndmask_b32_e64 v80, v98, v80, s[22:23]
	v_cndmask_b32_e64 v81, v99, v81, s[24:25]
	v_cndmask_b32_e64 v82, v100, v82, s[26:27]
	v_cndmask_b32_e64 v83, v101, v83, s[28:29]
	v_cndmask_b32_e64 v84, v102, v84, s[30:31]
	v_cndmask_b32_e64 v85, v103, v85, s[34:35]
	v_cndmask_b32_e64 v86, v104, v86, s[36:37]
	v_cndmask_b32_e64 v87, v105, v87, s[38:39]
	v_cndmask_b32_e64 v88, v106, v88, s[40:41]
	v_cndmask_b32_e64 v89, v107, v89, s[42:43]
	v_cndmask_b32_e64 v90, v108, v90, s[44:45]
	v_cndmask_b32_e64 v91, v109, v91, s[46:47]
	v_cndmask_b32_e64 v92, v110, v92, s[48:49]
	v_and_b32_e32 v77, 0xffffff80, v77
	v_and_b32_e32 v78, 0xffffff80, v78
	v_and_b32_e32 v79, 0xffffff80, v79
	v_and_b32_e32 v80, 0xffffff80, v80
	v_and_b32_e32 v81, 0xffffff80, v81
	v_and_b32_e32 v82, 0xffffff80, v82
	v_and_b32_e32 v83, 0xffffff80, v83
	v_and_b32_e32 v84, 0xffffff80, v84
	v_and_b32_e32 v85, 0xffffff80, v85
	v_and_b32_e32 v86, 0xffffff80, v86
	v_and_b32_e32 v87, 0xffffff80, v87
	v_and_b32_e32 v88, 0xffffff80, v88
	v_and_b32_e32 v89, 0xffffff80, v89
	v_and_b32_e32 v90, 0xffffff80, v90
	v_and_b32_e32 v91, 0xffffff80, v91
	v_and_b32_e32 v92, 0xffffff80, v92
	v_sub_u32_e32 v77, v77, v67
	v_sub_u32_e32 v78, v78, v67
	v_sub_u32_e32 v79, v79, v67
	v_sub_u32_e32 v80, v80, v67
	v_sub_u32_e32 v81, v81, v67
	v_sub_u32_e32 v82, v82, v67
	v_sub_u32_e32 v83, v83, v67
	v_sub_u32_e32 v84, v84, v67
	v_sub_u32_e32 v85, v85, v67
	v_sub_u32_e32 v86, v86, v67
	v_sub_u32_e32 v87, v87, v67
	v_sub_u32_e32 v88, v88, v67
	v_sub_u32_e32 v89, v89, v67
	v_sub_u32_e32 v90, v90, v67
	v_sub_u32_e32 v91, v91, v67
	v_sub_u32_e32 v92, v92, v67
	v_add_u32_e32 v77, 0x7f, v77
	v_add_u32_e32 v78, 0x7e, v78
	v_add_u32_e32 v79, 0x7d, v79
	v_add_u32_e32 v80, 0x7c, v80
	v_add_u32_e32 v81, 0x7b, v81
	v_add_u32_e32 v82, 0x7a, v82
	v_add_u32_e32 v83, 0x79, v83
	v_add_u32_e32 v84, 0x78, v84
	v_add_u32_e32 v85, 0x77, v85
	v_add_u32_e32 v86, 0x76, v86
	v_add_u32_e32 v87, 0x75, v87
	v_add_u32_e32 v88, 0x74, v88
	v_add_u32_e32 v89, 0x73, v89
	v_add_u32_e32 v90, 0x72, v90
	v_add_u32_e32 v91, 0x71, v91
	v_add_u32_e32 v92, 0x70, v92
	v_max_u32_e32 v93, v77, v78
	v_min_u32_e32 v77, v77, v78
	v_max_u32_e32 v78, v80, v79
	v_min_u32_e32 v79, v80, v79
	v_max_u32_e32 v80, v81, v82
	v_min_u32_e32 v81, v81, v82
	v_max_u32_e32 v82, v84, v83
	v_min_u32_e32 v83, v84, v83
	v_max_u32_e32 v84, v85, v86
	v_min_u32_e32 v85, v85, v86
	v_max_u32_e32 v86, v88, v87
	v_min_u32_e32 v87, v88, v87
	v_max_u32_e32 v88, v89, v90
	v_min_u32_e32 v89, v89, v90
	v_max_u32_e32 v90, v92, v91
	v_min_u32_e32 v91, v92, v91
	v_max_u32_e32 v92, v93, v79
	v_min_u32_e32 v79, v93, v79
	v_max_u32_e32 v93, v77, v78
	v_min_u32_e32 v77, v77, v78
	v_max_u32_e32 v78, v83, v80
	v_min_u32_e32 v80, v83, v80
	v_max_u32_e32 v83, v82, v81
	v_min_u32_e32 v81, v82, v81
	v_max_u32_e32 v82, v84, v87
	v_min_u32_e32 v84, v84, v87
	v_max_u32_e32 v87, v85, v86
	v_min_u32_e32 v85, v85, v86
	v_max_u32_e32 v86, v91, v88
	v_min_u32_e32 v88, v91, v88
	v_max_u32_e32 v91, v90, v89
	v_min_u32_e32 v89, v90, v89
	v_max_u32_e32 v90, v92, v93
	v_min_u32_e32 v92, v92, v93
	v_max_u32_e32 v93, v79, v77
	v_min_u32_e32 v77, v79, v77
	v_max_u32_e32 v79, v81, v80
	v_min_u32_e32 v80, v81, v80
	v_max_u32_e32 v81, v83, v78
	v_min_u32_e32 v78, v83, v78
	v_max_u32_e32 v83, v82, v87
	v_min_u32_e32 v82, v82, v87
	v_max_u32_e32 v87, v84, v85
	v_min_u32_e32 v84, v84, v85
	v_max_u32_e32 v85, v89, v88
	v_min_u32_e32 v88, v89, v88
	v_max_u32_e32 v89, v91, v86
	v_min_u32_e32 v86, v91, v86
	v_max_u32_e32 v91, v90, v80
	v_min_u32_e32 v80, v90, v80
	v_max_u32_e32 v90, v92, v79
	v_min_u32_e32 v79, v92, v79
	v_max_u32_e32 v92, v93, v78
; #define CE_DESC(x, y) do { const unsigned mx_ = (x) > (y) ? (x) : (y); const unsigned mn_ = (x) > (y) ? (y) : (x); (x) = mx_; (y) = mn_; } while (0)
; DI void sort16_desc(unsigned (&a)[16]) {
; #pragma unroll
;   for (int k = 2; k <= 16; k <<= 1)
; #pragma unroll
;     for (int j = k >> 1; j > 0; j >>= 1)
; #pragma unroll
;       for (int i = 0; i < 16; ++i) {
;         const int l = i ^ j;
;         if (l > i) { if ((i & k) == 0) CE_DESC(a[i], a[l]); else CE_DESC(a[l], a[i]); }
;       }
; }
; DI void merge16_desc(unsigned (&a)[16], const unsigned (&b)[16]) {
; #pragma unroll
;   for (int i = 0; i < 16; ++i) a[i] = a[i] > b[15 - i] ? a[i] : b[15 - i];
; #pragma unroll
;   for (int j = 8; j > 0; j >>= 1)
; #pragma unroll
;     for (int i = 0; i < 16; ++i) if ((i & j) == 0) CE_DESC(a[i], a[i + j]);
; }
; template <int CTRL> DI void dpp16(unsigned (&b)[16], const unsigned (&a)[16]) {
; #pragma unroll
;   for (int s = 0; s < 16; ++s) b[s] = (unsigned)__builtin_amdgcn_update_dpp(0, (int)a[s], CTRL, 0xF, 0xF, true);
; }
	v_min_u32_e32 v78, v93, v78
	v_max_u32_e32 v93, v77, v81
	v_min_u32_e32 v77, v77, v81
	v_max_u32_e32 v81, v88, v83
	v_min_u32_e32 v83, v88, v83
	v_max_u32_e32 v88, v85, v82
	v_min_u32_e32 v82, v85, v82
	v_max_u32_e32 v85, v86, v87
	v_min_u32_e32 v86, v86, v87
	v_max_u32_e32 v87, v89, v84
	v_min_u32_e32 v84, v89, v84
	v_max_u32_e32 v89, v91, v92
	v_min_u32_e32 v91, v91, v92
	v_max_u32_e32 v92, v90, v93
	v_min_u32_e32 v90, v90, v93
	v_max_u32_e32 v93, v80, v78
	v_min_u32_e32 v78, v80, v78
	v_max_u32_e32 v80, v79, v77
	v_min_u32_e32 v77, v79, v77
	v_max_u32_e32 v79, v86, v83
	v_min_u32_e32 v83, v86, v83
	v_max_u32_e32 v86, v84, v82
	v_min_u32_e32 v82, v84, v82
	v_max_u32_e32 v84, v85, v81
	v_min_u32_e32 v81, v85, v81
	v_max_u32_e32 v85, v87, v88
	v_min_u32_e32 v87, v87, v88
	v_max_u32_e32 v88, v89, v92
	v_min_u32_e32 v89, v89, v92
	v_max_u32_e32 v92, v91, v90
	v_min_u32_e32 v90, v91, v90
	v_max_u32_e32 v91, v93, v80
	v_min_u32_e32 v80, v93, v80
	v_max_u32_e32 v93, v78, v77
	v_min_u32_e32 v77, v78, v77
	v_max_u32_e32 v78, v82, v83
	v_min_u32_e32 v82, v82, v83
	v_max_u32_e32 v83, v86, v79
	v_min_u32_e32 v79, v86, v79
	v_max_u32_e32 v86, v87, v81
	v_min_u32_e32 v81, v87, v81
	v_max_u32_e32 v87, v85, v84
	v_min_u32_e32 v84, v85, v84
	v_max_u32_e32 v85, v88, v82
	v_min_u32_e32 v82, v88, v82
	v_max_u32_e32 v88, v89, v78
	v_min_u32_e32 v78, v89, v78
	v_max_u32_e32 v89, v92, v79
	v_min_u32_e32 v79, v92, v79
	v_max_u32_e32 v92, v90, v83
	v_min_u32_e32 v83, v90, v83
	v_max_u32_e32 v90, v91, v81
	v_min_u32_e32 v81, v91, v81
	v_max_u32_e32 v91, v80, v86
	v_min_u32_e32 v80, v80, v86
	v_max_u32_e32 v86, v93, v84
	v_min_u32_e32 v84, v93, v84
	v_max_u32_e32 v93, v77, v87
	v_min_u32_e32 v77, v77, v87
	v_max_u32_e32 v87, v85, v90
	v_min_u32_e32 v85, v85, v90
	v_max_u32_e32 v90, v88, v91
	v_min_u32_e32 v88, v88, v91
	v_max_u32_e32 v91, v89, v86
	v_min_u32_e32 v86, v89, v86
	v_max_u32_e32 v89, v92, v93
	v_min_u32_e32 v92, v92, v93
	v_max_u32_e32 v93, v82, v81
	v_min_u32_e32 v81, v82, v81
	v_max_u32_e32 v82, v78, v80
	v_min_u32_e32 v78, v78, v80
	v_max_u32_e32 v80, v79, v84
	v_min_u32_e32 v79, v79, v84
	v_max_u32_e32 v84, v83, v77
	v_min_u32_e32 v77, v83, v77
	v_max_u32_e32 v83, v87, v91
	v_min_u32_e32 v87, v87, v91
	v_max_u32_e32 v91, v90, v89
	v_min_u32_e32 v89, v90, v89
	v_max_u32_e32 v90, v85, v86
	v_min_u32_e32 v85, v85, v86
	v_max_u32_e32 v86, v88, v92
	v_min_u32_e32 v88, v88, v92
	v_max_u32_e32 v92, v93, v80
	v_min_u32_e32 v80, v93, v80
	v_max_u32_e32 v93, v82, v84
	v_min_u32_e32 v82, v82, v84
	v_max_u32_e32 v84, v81, v79
	v_min_u32_e32 v79, v81, v79
	v_max_u32_e32 v81, v78, v77
	v_min_u32_e32 v77, v78, v77
	v_max_u32_e32 v78, v83, v91
	v_min_u32_e32 v83, v83, v91
	v_max_u32_e32 v91, v87, v89
	v_min_u32_e32 v87, v87, v89
	v_max_u32_e32 v89, v90, v86
	v_min_u32_e32 v86, v90, v86
	v_max_u32_e32 v90, v85, v88
	v_min_u32_e32 v85, v85, v88
	v_max_u32_e32 v88, v92, v93
	v_min_u32_e32 v92, v92, v93
	v_max_u32_e32 v93, v80, v82
	v_min_u32_e32 v80, v80, v82
	v_max_u32_e32 v82, v84, v81
	v_min_u32_e32 v81, v84, v81
	v_max_u32_e32 v84, v79, v77
	v_min_u32_e32 v77, v79, v77
	v_mov_b32_dpp v79, v78 quad_perm:[1,0,3,2] row_mask:0xf bank_mask:0xf bound_ctrl:1
	v_mov_b32_dpp v94, v83 quad_perm:[1,0,3,2] row_mask:0xf bank_mask:0xf bound_ctrl:1
	v_mov_b32_dpp v95, v91 quad_perm:[1,0,3,2] row_mask:0xf bank_mask:0xf bound_ctrl:1
	v_mov_b32_dpp v96, v87 quad_perm:[1,0,3,2] row_mask:0xf bank_mask:0xf bound_ctrl:1
	v_mov_b32_dpp v97, v89 quad_perm:[1,0,3,2] row_mask:0xf bank_mask:0xf bound_ctrl:1
	v_mov_b32_dpp v98, v86 quad_perm:[1,0,3,2] row_mask:0xf bank_mask:0xf bound_ctrl:1
	v_max_u32_dpp v78, v77, v78 quad_perm:[1,0,3,2] row_mask:0xf bank_mask:0xf bound_ctrl:1
	v_max_u32_dpp v83, v84, v83 quad_perm:[1,0,3,2] row_mask:0xf bank_mask:0xf bound_ctrl:1
	v_max_u32_dpp v91, v81, v91 quad_perm:[1,0,3,2] row_mask:0xf bank_mask:0xf bound_ctrl:1
	v_max_u32_dpp v87, v82, v87 quad_perm:[1,0,3,2] row_mask:0xf bank_mask:0xf bound_ctrl:1
	v_max_u32_dpp v89, v80, v89 quad_perm:[1,0,3,2] row_mask:0xf bank_mask:0xf bound_ctrl:1
	v_max_u32_dpp v86, v93, v86 quad_perm:[1,0,3,2] row_mask:0xf bank_mask:0xf bound_ctrl:1
	v_max_u32_dpp v99, v92, v90 quad_perm:[1,0,3,2] row_mask:0xf bank_mask:0xf bound_ctrl:1
	v_max_u32_dpp v100, v88, v85 quad_perm:[1,0,3,2] row_mask:0xf bank_mask:0xf bound_ctrl:1
	v_max_u32_dpp v85, v85, v88 quad_perm:[1,0,3,2] row_mask:0xf bank_mask:0xf bound_ctrl:1
	v_max_u32_dpp v88, v90, v92 quad_perm:[1,0,3,2] row_mask:0xf bank_mask:0xf bound_ctrl:1
	v_max_u32_e32 v90, v93, v98
	v_max_u32_e32 v80, v80, v97
	v_max_u32_e32 v82, v82, v96
	v_max_u32_e32 v81, v81, v95
	v_max_u32_e32 v84, v84, v94
	v_max_u32_e32 v77, v77, v79
	v_max_u32_e32 v79, v78, v85
	v_min_u32_e32 v78, v78, v85
	v_max_u32_e32 v85, v83, v88
	v_min_u32_e32 v83, v83, v88
	v_max_u32_e32 v88, v91, v90
	v_min_u32_e32 v90, v91, v90
	v_max_u32_e32 v91, v87, v80
	v_min_u32_e32 v80, v87, v80
	v_max_u32_e32 v87, v89, v82
	v_min_u32_e32 v82, v89, v82
	v_max_u32_e32 v89, v86, v81
	v_min_u32_e32 v81, v86, v81
	v_max_u32_e32 v86, v99, v84
	v_max_u32_e32 v92, v100, v77
	v_min_u32_e32 v84, v99, v84
	v_min_u32_e32 v77, v100, v77
	v_max_u32_e32 v93, v79, v87
	v_min_u32_e32 v79, v79, v87
	v_max_u32_e32 v87, v85, v89
	v_min_u32_e32 v85, v85, v89
	v_max_u32_e32 v89, v88, v86
	v_min_u32_e32 v86, v88, v86
	v_max_u32_e32 v88, v91, v92
	v_min_u32_e32 v91, v91, v92
	v_max_u32_e32 v92, v78, v82
	v_min_u32_e32 v78, v78, v82
	v_max_u32_e32 v82, v83, v81
	v_min_u32_e32 v81, v83, v81
	v_max_u32_e32 v83, v90, v84
	v_min_u32_e32 v84, v90, v84
	v_max_u32_e32 v90, v80, v77
	v_min_u32_e32 v77, v80, v77
	v_max_u32_e32 v80, v93, v89
; #define CE_DESC(x, y) do { const unsigned mx_ = (x) > (y) ? (x) : (y); const unsigned mn_ = (x) > (y) ? (y) : (x); (x) = mx_; (y) = mn_; } while (0)
; DI void merge16_desc(unsigned (&a)[16], const unsigned (&b)[16]) {
; #pragma unroll
;   for (int i = 0; i < 16; ++i) a[i] = a[i] > b[15 - i] ? a[i] : b[15 - i];
; #pragma unroll
;   for (int j = 8; j > 0; j >>= 1)
; #pragma unroll
;     for (int i = 0; i < 16; ++i) if ((i & j) == 0) CE_DESC(a[i], a[i + j]);
; }
; template <int CTRL> DI void dpp16(unsigned (&b)[16], const unsigned (&a)[16]) {
; #pragma unroll
;   for (int s = 0; s < 16; ++s) b[s] = (unsigned)__builtin_amdgcn_update_dpp(0, (int)a[s], CTRL, 0xF, 0xF, true);
; }
	v_min_u32_e32 v89, v93, v89
	v_max_u32_e32 v93, v87, v88
	v_min_u32_e32 v87, v87, v88
	v_max_u32_e32 v88, v79, v86
	v_min_u32_e32 v79, v79, v86
	v_max_u32_e32 v86, v85, v91
	v_min_u32_e32 v85, v85, v91
	v_max_u32_e32 v91, v92, v83
	v_min_u32_e32 v83, v92, v83
	v_max_u32_e32 v92, v82, v90
	v_min_u32_e32 v82, v82, v90
	v_max_u32_e32 v90, v78, v84
	v_min_u32_e32 v78, v78, v84
	v_max_u32_e32 v84, v81, v77
	v_min_u32_e32 v77, v81, v77
	v_max_u32_e32 v81, v80, v93
	v_min_u32_e32 v80, v80, v93
	v_max_u32_e32 v93, v89, v87
	v_min_u32_e32 v87, v89, v87
	v_max_u32_e32 v89, v88, v86
	v_min_u32_e32 v86, v88, v86
	v_max_u32_e32 v88, v79, v85
	v_min_u32_e32 v79, v79, v85
	v_max_u32_e32 v85, v91, v92
	v_min_u32_e32 v91, v91, v92
	v_max_u32_e32 v92, v83, v82
	v_min_u32_e32 v82, v83, v82
	v_max_u32_e32 v83, v90, v84
	v_min_u32_e32 v84, v90, v84
	v_max_u32_e32 v90, v78, v77
	v_min_u32_e32 v77, v78, v77
	v_mov_b32_dpp v78, v81 quad_perm:[2,3,0,1] row_mask:0xf bank_mask:0xf bound_ctrl:1
	v_mov_b32_dpp v94, v80 quad_perm:[2,3,0,1] row_mask:0xf bank_mask:0xf bound_ctrl:1
	v_mov_b32_dpp v95, v93 quad_perm:[2,3,0,1] row_mask:0xf bank_mask:0xf bound_ctrl:1
	v_mov_b32_dpp v96, v87 quad_perm:[2,3,0,1] row_mask:0xf bank_mask:0xf bound_ctrl:1
	v_mov_b32_dpp v97, v89 quad_perm:[2,3,0,1] row_mask:0xf bank_mask:0xf bound_ctrl:1
	v_mov_b32_dpp v98, v86 quad_perm:[2,3,0,1] row_mask:0xf bank_mask:0xf bound_ctrl:1
	v_max_u32_dpp v81, v77, v81 quad_perm:[2,3,0,1] row_mask:0xf bank_mask:0xf bound_ctrl:1
	v_max_u32_dpp v80, v90, v80 quad_perm:[2,3,0,1] row_mask:0xf bank_mask:0xf bound_ctrl:1
	v_max_u32_dpp v93, v84, v93 quad_perm:[2,3,0,1] row_mask:0xf bank_mask:0xf bound_ctrl:1
	v_max_u32_dpp v87, v83, v87 quad_perm:[2,3,0,1] row_mask:0xf bank_mask:0xf bound_ctrl:1
	v_max_u32_dpp v89, v82, v89 quad_perm:[2,3,0,1] row_mask:0xf bank_mask:0xf bound_ctrl:1
	v_max_u32_dpp v86, v92, v86 quad_perm:[2,3,0,1] row_mask:0xf bank_mask:0xf bound_ctrl:1
	v_max_u32_dpp v99, v91, v88 quad_perm:[2,3,0,1] row_mask:0xf bank_mask:0xf bound_ctrl:1
	v_max_u32_dpp v100, v85, v79 quad_perm:[2,3,0,1] row_mask:0xf bank_mask:0xf bound_ctrl:1
	v_max_u32_dpp v79, v79, v85 quad_perm:[2,3,0,1] row_mask:0xf bank_mask:0xf bound_ctrl:1
	v_max_u32_dpp v85, v88, v91 quad_perm:[2,3,0,1] row_mask:0xf bank_mask:0xf bound_ctrl:1
	v_max_u32_e32 v88, v92, v98
	v_max_u32_e32 v82, v82, v97
	v_max_u32_e32 v83, v83, v96
	v_max_u32_e32 v84, v84, v95
	v_max_u32_e32 v90, v90, v94
	v_max_u32_e32 v77, v77, v78
	v_max_u32_e32 v78, v81, v79
	v_min_u32_e32 v79, v81, v79
	v_max_u32_e32 v81, v80, v85
	v_min_u32_e32 v80, v80, v85
	v_max_u32_e32 v85, v93, v88
	v_max_u32_e32 v91, v87, v82
	v_min_u32_e32 v82, v87, v82
	v_max_u32_e32 v87, v89, v83
	v_min_u32_e32 v83, v89, v83
	v_max_u32_e32 v89, v86, v84
	v_min_u32_e32 v84, v86, v84
	v_max_u32_e32 v86, v99, v90
	v_max_u32_e32 v92, v100, v77
	v_min_u32_e32 v88, v93, v88
	v_min_u32_e32 v90, v99, v90
	v_min_u32_e32 v77, v100, v77
	v_max_u32_e32 v93, v78, v87
	v_min_u32_e32 v78, v78, v87
	v_max_u32_e32 v87, v81, v89
	v_min_u32_e32 v81, v81, v89
	v_max_u32_e32 v89, v85, v86
	v_min_u32_e32 v85, v85, v86
	v_max_u32_e32 v86, v91, v92
	v_min_u32_e32 v91, v91, v92
	v_max_u32_e32 v92, v79, v83
	v_min_u32_e32 v79, v79, v83
	v_max_u32_e32 v83, v80, v84
	v_min_u32_e32 v80, v80, v84
	v_max_u32_e32 v84, v88, v90
	v_min_u32_e32 v88, v88, v90
	v_max_u32_e32 v90, v82, v77
	v_min_u32_e32 v77, v82, v77
	v_max_u32_e32 v82, v93, v89
	v_min_u32_e32 v89, v93, v89
	v_max_u32_e32 v93, v87, v86
	v_min_u32_e32 v86, v87, v86
	v_max_u32_e32 v87, v78, v85
	v_min_u32_e32 v78, v78, v85
	v_max_u32_e32 v85, v81, v91
	v_min_u32_e32 v81, v81, v91
	v_max_u32_e32 v91, v92, v84
	v_min_u32_e32 v84, v92, v84
	v_max_u32_e32 v92, v83, v90
	v_min_u32_e32 v83, v83, v90
	v_max_u32_e32 v90, v79, v88
	v_min_u32_e32 v79, v79, v88
	v_max_u32_e32 v88, v80, v77
	v_min_u32_e32 v77, v80, v77
	v_max_u32_e32 v80, v82, v93
	v_min_u32_e32 v82, v82, v93
	v_max_u32_e32 v93, v89, v86
	v_min_u32_e32 v86, v89, v86
	v_max_u32_e32 v89, v87, v85
	v_min_u32_e32 v85, v87, v85
	v_max_u32_e32 v87, v78, v81
	v_min_u32_e32 v78, v78, v81
	v_max_u32_e32 v81, v91, v92
	v_min_u32_e32 v91, v91, v92
	v_max_u32_e32 v92, v84, v83
	v_min_u32_e32 v83, v84, v83
	v_max_u32_e32 v84, v90, v88
	v_min_u32_e32 v88, v90, v88
	v_max_u32_e32 v90, v79, v77
	v_min_u32_e32 v77, v79, v77
	v_mov_b32_dpp v79, v80 row_half_mirror row_mask:0xf bank_mask:0xf bound_ctrl:1
	v_mov_b32_dpp v94, v82 row_half_mirror row_mask:0xf bank_mask:0xf bound_ctrl:1
	v_mov_b32_dpp v95, v93 row_half_mirror row_mask:0xf bank_mask:0xf bound_ctrl:1
	v_mov_b32_dpp v96, v86 row_half_mirror row_mask:0xf bank_mask:0xf bound_ctrl:1
	v_mov_b32_dpp v97, v89 row_half_mirror row_mask:0xf bank_mask:0xf bound_ctrl:1
	v_mov_b32_dpp v98, v85 row_half_mirror row_mask:0xf bank_mask:0xf bound_ctrl:1
	v_max_u32_dpp v80, v77, v80 row_half_mirror row_mask:0xf bank_mask:0xf bound_ctrl:1
	v_max_u32_dpp v82, v90, v82 row_half_mirror row_mask:0xf bank_mask:0xf bound_ctrl:1
	v_max_u32_dpp v93, v88, v93 row_half_mirror row_mask:0xf bank_mask:0xf bound_ctrl:1
	v_max_u32_dpp v86, v84, v86 row_half_mirror row_mask:0xf bank_mask:0xf bound_ctrl:1
	v_max_u32_dpp v89, v83, v89 row_half_mirror row_mask:0xf bank_mask:0xf bound_ctrl:1
	v_max_u32_dpp v85, v92, v85 row_half_mirror row_mask:0xf bank_mask:0xf bound_ctrl:1
	v_max_u32_dpp v99, v91, v87 row_half_mirror row_mask:0xf bank_mask:0xf bound_ctrl:1
	v_max_u32_dpp v100, v81, v78 row_half_mirror row_mask:0xf bank_mask:0xf bound_ctrl:1
	v_max_u32_dpp v78, v78, v81 row_half_mirror row_mask:0xf bank_mask:0xf bound_ctrl:1
	v_max_u32_dpp v81, v87, v91 row_half_mirror row_mask:0xf bank_mask:0xf bound_ctrl:1
; DI unsigned ordkey(float f) { const unsigned u = __float_as_uint(f); return (u & 0x80000000u) ? ~u : (u | 0x80000000u); }
; DI void peer_select_unit(const Params& p, int unit, char* lds, const bf16x8 (&kb)[4][4]) {
;     ...
;     dpp16<0x141>(bq, a); merge16_desc(a, bq);
; #pragma unroll
;     for (int s = 0; s < 2; ++s) {
;       unsigned k = 0u;
; #pragma unroll
;       for (int q = 0; q < 8; ++q) k = part == q ? a[2 * q + s] : k;
;       const int idx = 127 - (int)(k & 127u);
;       topv[rr * 16 + 2 * part + s] = sc[rr * 132 + idx]; topi[rr * 16 + 2 * part + s] = idx;
;     }
;   }
;   __syncthreads();
;   if (tid < 128) {
;     const int tok = tid >> 2, q4 = tid & 3;
;     unsigned c[16], bq[16];
; #pragma unroll
;     for (int i = 0; i < 16; ++i) {
;       const unsigned code = PEER_CAND[16 * q4 + i];
;       const float v = topv[tok * 16 + ((code >> 4) & 15)] + topv[(32 + tok) * 16 + (code & 15)];
;       c[i] = code == 0xFFu ? 0u : ((ordkey(v) & ~255u) | (255u - code));
	v_max_u32_e32 v87, v92, v98
	v_max_u32_e32 v83, v83, v97
	v_max_u32_e32 v84, v84, v96
	v_max_u32_e32 v88, v88, v95
	v_max_u32_e32 v90, v90, v94
	v_max_u32_e32 v77, v77, v79
	v_max_u32_e32 v79, v80, v78
	v_min_u32_e32 v78, v80, v78
	v_max_u32_e32 v80, v82, v81
	v_min_u32_e32 v81, v82, v81
	v_max_u32_e32 v82, v93, v87
	v_max_u32_e32 v91, v86, v83
	v_min_u32_e32 v83, v86, v83
	v_max_u32_e32 v86, v89, v84
	v_min_u32_e32 v84, v89, v84
	v_max_u32_e32 v89, v85, v88
	v_min_u32_e32 v85, v85, v88
	v_max_u32_e32 v88, v99, v90
	v_max_u32_e32 v92, v100, v77
	v_min_u32_e32 v87, v93, v87
	v_min_u32_e32 v90, v99, v90
	v_min_u32_e32 v77, v100, v77
	v_max_u32_e32 v93, v79, v86
	v_min_u32_e32 v79, v79, v86
	v_max_u32_e32 v86, v80, v89
	v_min_u32_e32 v80, v80, v89
	v_max_u32_e32 v89, v82, v88
	v_min_u32_e32 v82, v82, v88
	v_max_u32_e32 v88, v91, v92
	v_min_u32_e32 v91, v91, v92
	v_max_u32_e32 v92, v78, v84
	v_min_u32_e32 v78, v78, v84
	v_max_u32_e32 v84, v81, v85
	v_min_u32_e32 v81, v81, v85
	v_max_u32_e32 v85, v87, v90
	v_min_u32_e32 v87, v87, v90
	v_max_u32_e32 v90, v83, v77
	v_min_u32_e32 v77, v83, v77
	v_max_u32_e32 v83, v93, v89
	v_min_u32_e32 v89, v93, v89
	v_max_u32_e32 v93, v86, v88
	v_min_u32_e32 v86, v86, v88
	v_max_u32_e32 v88, v79, v82
	v_min_u32_e32 v79, v79, v82
	v_max_u32_e32 v82, v80, v91
	v_min_u32_e32 v80, v80, v91
	v_max_u32_e32 v91, v92, v85
	v_min_u32_e32 v85, v92, v85
	v_max_u32_e32 v92, v84, v90
	v_min_u32_e32 v84, v84, v90
	v_max_u32_e32 v90, v78, v87
	v_min_u32_e32 v78, v78, v87
	v_max_u32_e32 v87, v81, v77
	v_min_u32_e32 v77, v81, v77
	v_max_u32_e32 v81, v83, v93
	v_min_u32_e32 v83, v83, v93
	v_max_u32_e32 v93, v89, v86
	v_min_u32_e32 v86, v89, v86
	v_max_u32_e32 v89, v88, v82
	v_min_u32_e32 v82, v88, v82
	v_max_u32_e32 v88, v79, v80
	v_min_u32_e32 v79, v79, v80
	v_max_u32_e32 v80, v91, v92
	v_min_u32_e32 v91, v91, v92
	v_max_u32_e32 v92, v85, v84
	v_min_u32_e32 v84, v85, v84
	v_max_u32_e32 v85, v90, v87
	v_min_u32_e32 v87, v90, v87
	v_max_u32_e32 v90, v78, v77
	v_min_u32_e32 v77, v78, v77
	v_cndmask_b32_e64 v78, 0, v81, s[0:1]
	v_cndmask_b32_e64 v78, v78, v93, s[4:5]
	v_cndmask_b32_e64 v78, v78, v89, s[6:7]
	v_cndmask_b32_e64 v78, v78, v88, s[8:9]
	v_cndmask_b32_e64 v78, v78, v80, s[10:11]
	v_cndmask_b32_e64 v78, v78, v92, s[12:13]
	v_cndmask_b32_e64 v81, 0, v83, s[0:1]
	v_cndmask_b32_e64 v78, v78, v85, s[14:15]
	v_cndmask_b32_e64 v81, v81, v86, s[4:5]
	v_cndmask_b32_e64 v78, v78, v90, s[16:17]
	v_cndmask_b32_e64 v81, v81, v82, s[6:7]
	v_bitop3_b32 v78, v78, s3, v78 bitop3:0xc
	v_cndmask_b32_e64 v79, v81, v79, s[8:9]
	v_lshlrev_b32_e32 v80, 2, v78
	v_cndmask_b32_e64 v79, v79, v91, s[10:11]
	v_add3_u32 v80, v146, v80, v76
	v_cndmask_b32_e64 v79, v79, v84, s[12:13]
	ds_read_b32 v80, v80
	v_cndmask_b32_e64 v79, v79, v87, s[14:15]
	v_cndmask_b32_e64 v77, v79, v77, s[16:17]
	v_lshl_or_b32 v71, v71, 6, v69
	v_bitop3_b32 v79, v77, s3, v77 bitop3:0xc
	v_add_u32_e32 v71, v146, v71
	v_lshlrev_b32_e32 v77, 2, v79
	v_add3_u32 v76, v146, v77, v76
	s_waitcnt lgkmcnt(0)
	ds_write_b32 v71, v80 offset:33792
	ds_read_b32 v76, v76
	v_cmp_ne_u32_e32 vcc, 1, v70
	s_mov_b32 s69, 32
	s_mov_b64 s[20:21], 0
	ds_write_b64 v71, v[78:79] offset:37888
	s_waitcnt lgkmcnt(1)
	ds_write_b32 v71, v76 offset:33796
	s_cbranch_vccz .LBB0_1653
	v_xor_b32_e32 v66, v249, v66
	v_cmp_gt_i32_e32 vcc, s18, v66
	s_waitcnt lgkmcnt(0)
	s_barrier
	s_and_saveexec_b64 s[8:9], vcc
	s_cbranch_execz .LBB0_1651
	v_and_b32_e32 v77, 3, v66
	v_lshrrev_b32_e32 v75, 2, v66
	v_lshlrev_b32_e32 v64, 4, v77
	v_and_b32_e32 v80, 0xffff, v244
	v_lshlrev_b32_e32 v66, 6, v75
	v_lshlrev_b32_e32 v76, 4, v75
	v_cmp_eq_u32_e32 vcc, 3, v77
	v_cmp_ne_u32_e64 s[0:1], 3, v77
	v_mov_b32_e32 v82, 0
	v_lshrrev_b32_e32 v67, 2, v80
	v_and_b32_e32 v68, 15, v80
	v_lshrrev_b16_e32 v79, 8, v80
	v_and_b32_e32 v67, 60, v67
	v_lshlrev_b32_e32 v68, 2, v68
	v_lshrrev_b32_e32 v69, 2, v79
	v_and_b32_e32 v78, 15, v79
	v_add3_u32 v67, v146, v67, v66
	v_add3_u32 v68, v146, v68, v66
	v_and_b32_e32 v69, 60, v69
	v_lshlrev_b32_e32 v78, 2, v78
	v_add3_u32 v81, v146, v69, v66
	v_add3_u32 v78, v146, v78, v66
	ds_read_b32 v67, v67 offset:33792
	ds_read_b32 v69, v68 offset:35840
	ds_read_b32 v66, v81 offset:33792
	ds_read_b32 v68, v78 offset:35840
	v_mov_b32_e32 v81, 0
	v_lshlrev_b32_e32 v78, 2, v76
	v_mov_b32_e32 v83, 0
	v_mov_b32_e32 v84, 0
	v_mov_b32_e32 v85, 0
	v_mov_b32_e32 v86, 0
	v_mov_b32_e32 v87, 0
	v_mov_b32_e32 v88, 0
	v_mov_b32_e32 v89, 0
	v_mov_b32_e32 v90, 0
	v_mov_b32_e32 v91, 0
	v_mov_b32_e32 v92, 0
	v_mov_b32_e32 v93, 0
	v_mov_b32_e32 v94, 0
	s_and_saveexec_b64 s[6:7], s[0:1]
	v_bfe_u32 v82, v244, 16, 8
	v_lshrrev_b32_e32 v238, 2, v82
	v_and_b32_e32 v239, 15, v82
	v_and_b32_e32 v238, 60, v238
	v_lshlrev_b32_e32 v239, 2, v239
	v_add3_u32 v238, v146, v238, v78
	v_add3_u32 v239, v146, v239, v78
	ds_read_b32 v210, v238 offset:33792
	ds_read_b32 v211, v239 offset:35840
	v_bfe_u32 v81, v244, 24, 8
	v_lshrrev_b32_e32 v238, 2, v81
	v_and_b32_e32 v239, 15, v81
	v_and_b32_e32 v238, 60, v238
	v_lshlrev_b32_e32 v239, 2, v239
	v_add3_u32 v238, v146, v238, v78
	v_add3_u32 v239, v146, v239, v78
	ds_read_b32 v212, v238 offset:33792
	ds_read_b32 v213, v239 offset:35840
	v_bfe_u32 v84, v245, 0, 8
	v_lshrrev_b32_e32 v238, 2, v84
	v_and_b32_e32 v239, 15, v84
	v_and_b32_e32 v238, 60, v238
	v_lshlrev_b32_e32 v239, 2, v239
	v_add3_u32 v238, v146, v238, v78
	v_add3_u32 v239, v146, v239, v78
	ds_read_b32 v214, v238 offset:33792
	ds_read_b32 v215, v239 offset:35840
	v_bfe_u32 v83, v245, 8, 8
	v_lshrrev_b32_e32 v238, 2, v83
	v_and_b32_e32 v239, 15, v83
	v_and_b32_e32 v238, 60, v238
	v_lshlrev_b32_e32 v239, 2, v239
	v_add3_u32 v238, v146, v238, v78
; DI unsigned ordkey(float f) { const unsigned u = __float_as_uint(f); return (u & 0x80000000u) ? ~u : (u | 0x80000000u); }
; DI void peer_select_unit(const Params& p, int unit, char* lds, const bf16x8 (&kb)[4][4]) {
;     ...
; #pragma unroll
;     for (int i = 0; i < 16; ++i) {
;       const unsigned code = PEER_CAND[16 * q4 + i];
;       const float v = topv[tok * 16 + ((code >> 4) & 15)] + topv[(32 + tok) * 16 + (code & 15)];
;       c[i] = code == 0xFFu ? 0u : ((ordkey(v) & ~255u) | (255u - code));
	v_add3_u32 v239, v146, v239, v78
	ds_read_b32 v216, v238 offset:33792
	ds_read_b32 v217, v239 offset:35840
	v_bfe_u32 v86, v245, 16, 8
	v_lshrrev_b32_e32 v238, 2, v86
	v_and_b32_e32 v239, 15, v86
	v_and_b32_e32 v238, 60, v238
	v_lshlrev_b32_e32 v239, 2, v239
	v_add3_u32 v238, v146, v238, v78
	v_add3_u32 v239, v146, v239, v78
	ds_read_b32 v218, v238 offset:33792
	ds_read_b32 v219, v239 offset:35840
	v_bfe_u32 v85, v245, 24, 8
	v_lshrrev_b32_e32 v238, 2, v85
	v_and_b32_e32 v239, 15, v85
	v_and_b32_e32 v238, 60, v238
	v_lshlrev_b32_e32 v239, 2, v239
	v_add3_u32 v238, v146, v238, v78
	v_add3_u32 v239, v146, v239, v78
	ds_read_b32 v220, v238 offset:33792
	ds_read_b32 v221, v239 offset:35840
	v_bfe_u32 v88, v246, 0, 8
	v_lshrrev_b32_e32 v238, 2, v88
	v_and_b32_e32 v239, 15, v88
	v_and_b32_e32 v238, 60, v238
	v_lshlrev_b32_e32 v239, 2, v239
	v_add3_u32 v238, v146, v238, v78
	v_add3_u32 v239, v146, v239, v78
	ds_read_b32 v222, v238 offset:33792
	ds_read_b32 v223, v239 offset:35840
	v_bfe_u32 v87, v246, 8, 8
	v_lshrrev_b32_e32 v238, 2, v87
	v_and_b32_e32 v239, 15, v87
	v_and_b32_e32 v238, 60, v238
	v_lshlrev_b32_e32 v239, 2, v239
	v_add3_u32 v238, v146, v238, v78
	v_add3_u32 v239, v146, v239, v78
	ds_read_b32 v224, v238 offset:33792
	ds_read_b32 v225, v239 offset:35840
	v_bfe_u32 v90, v246, 16, 8
	v_lshrrev_b32_e32 v238, 2, v90
	v_and_b32_e32 v239, 15, v90
	v_and_b32_e32 v238, 60, v238
	v_lshlrev_b32_e32 v239, 2, v239
	v_add3_u32 v238, v146, v238, v78
	v_add3_u32 v239, v146, v239, v78
	ds_read_b32 v226, v238 offset:33792
	ds_read_b32 v227, v239 offset:35840
	v_bfe_u32 v89, v246, 24, 8
	v_lshrrev_b32_e32 v238, 2, v89
	v_and_b32_e32 v239, 15, v89
	v_and_b32_e32 v238, 60, v238
	v_lshlrev_b32_e32 v239, 2, v239
	v_add3_u32 v238, v146, v238, v78
	v_add3_u32 v239, v146, v239, v78
	ds_read_b32 v228, v238 offset:33792
	ds_read_b32 v229, v239 offset:35840
	v_bfe_u32 v92, v247, 0, 8
	v_lshrrev_b32_e32 v238, 2, v92
	v_and_b32_e32 v239, 15, v92
	v_and_b32_e32 v238, 60, v238
	v_lshlrev_b32_e32 v239, 2, v239
	v_add3_u32 v238, v146, v238, v78
	v_add3_u32 v239, v146, v239, v78
	ds_read_b32 v230, v238 offset:33792
	ds_read_b32 v231, v239 offset:35840
	v_bfe_u32 v91, v247, 8, 8
	v_lshrrev_b32_e32 v238, 2, v91
	v_and_b32_e32 v239, 15, v91
	v_and_b32_e32 v238, 60, v238
	v_lshlrev_b32_e32 v239, 2, v239
	v_add3_u32 v238, v146, v238, v78
	v_add3_u32 v239, v146, v239, v78
	ds_read_b32 v232, v238 offset:33792
	ds_read_b32 v233, v239 offset:35840
	v_bfe_u32 v94, v247, 16, 8
	v_lshrrev_b32_e32 v238, 2, v94
	v_and_b32_e32 v239, 15, v94
	v_and_b32_e32 v238, 60, v238
	v_lshlrev_b32_e32 v239, 2, v239
	v_add3_u32 v238, v146, v238, v78
	v_add3_u32 v239, v146, v239, v78
	ds_read_b32 v234, v238 offset:33792
	ds_read_b32 v235, v239 offset:35840
	v_bfe_u32 v70, v247, 24, 8
	v_lshrrev_b32_e32 v238, 2, v70
	v_and_b32_e32 v239, 15, v70
	v_and_b32_e32 v238, 60, v238
	v_lshlrev_b32_e32 v239, 2, v239
	v_add3_u32 v238, v146, v238, v78
	v_add3_u32 v239, v146, v239, v78
	ds_read_b32 v236, v238 offset:33792
	ds_read_b32 v237, v239 offset:35840
	s_waitcnt lgkmcnt(0)
	v_add_f32_e32 v210, v210, v211
	v_cmp_gt_i32_e64 s[4:5], 0, v210
	v_not_b32_e32 v211, v210
	v_or_b32_e32 v238, 0x80000000, v210
	v_cndmask_b32_e64 v210, v238, v211, s[4:5]
	v_and_b32_e32 v210, 0xffffff00, v210
	v_bitop3_b32 v82, v210, s19, v82 bitop3:0x36
	v_add_f32_e32 v212, v212, v213
	v_cmp_gt_i32_e64 s[4:5], 0, v212
	v_not_b32_e32 v213, v212
	v_or_b32_e32 v238, 0x80000000, v212
	v_cndmask_b32_e64 v212, v238, v213, s[4:5]
	v_and_b32_e32 v212, 0xffffff00, v212
	v_bitop3_b32 v81, v212, s19, v81 bitop3:0x36
	v_add_f32_e32 v214, v214, v215
	v_cmp_gt_i32_e64 s[4:5], 0, v214
	v_not_b32_e32 v215, v214
	v_or_b32_e32 v238, 0x80000000, v214
	v_cndmask_b32_e64 v214, v238, v215, s[4:5]
	v_and_b32_e32 v214, 0xffffff00, v214
	v_bitop3_b32 v84, v214, s19, v84 bitop3:0x36
	v_add_f32_e32 v216, v216, v217
	v_cmp_gt_i32_e64 s[4:5], 0, v216
	v_not_b32_e32 v217, v216
	v_or_b32_e32 v238, 0x80000000, v216
	v_cndmask_b32_e64 v216, v238, v217, s[4:5]
	v_and_b32_e32 v216, 0xffffff00, v216
	v_bitop3_b32 v83, v216, s19, v83 bitop3:0x36
	v_add_f32_e32 v218, v218, v219
	v_cmp_gt_i32_e64 s[4:5], 0, v218
	v_not_b32_e32 v219, v218
	v_or_b32_e32 v238, 0x80000000, v218
	v_cndmask_b32_e64 v218, v238, v219, s[4:5]
	v_and_b32_e32 v218, 0xffffff00, v218
	v_bitop3_b32 v86, v218, s19, v86 bitop3:0x36
	v_add_f32_e32 v220, v220, v221
	v_cmp_gt_i32_e64 s[4:5], 0, v220
	v_not_b32_e32 v221, v220
	v_or_b32_e32 v238, 0x80000000, v220
	v_cndmask_b32_e64 v220, v238, v221, s[4:5]
	v_and_b32_e32 v220, 0xffffff00, v220
	v_bitop3_b32 v85, v220, s19, v85 bitop3:0x36
	v_add_f32_e32 v222, v222, v223
	v_cmp_gt_i32_e64 s[4:5], 0, v222
	v_not_b32_e32 v223, v222
	v_or_b32_e32 v238, 0x80000000, v222
	v_cndmask_b32_e64 v222, v238, v223, s[4:5]
	v_and_b32_e32 v222, 0xffffff00, v222
	v_bitop3_b32 v88, v222, s19, v88 bitop3:0x36
	v_add_f32_e32 v224, v224, v225
	v_cmp_gt_i32_e64 s[4:5], 0, v224
	v_not_b32_e32 v225, v224
	v_or_b32_e32 v238, 0x80000000, v224
	v_cndmask_b32_e64 v224, v238, v225, s[4:5]
	v_and_b32_e32 v224, 0xffffff00, v224
	v_bitop3_b32 v87, v224, s19, v87 bitop3:0x36
	v_add_f32_e32 v226, v226, v227
	v_cmp_gt_i32_e64 s[4:5], 0, v226
	v_not_b32_e32 v227, v226
	v_or_b32_e32 v238, 0x80000000, v226
	v_cndmask_b32_e64 v226, v238, v227, s[4:5]
	v_and_b32_e32 v226, 0xffffff00, v226
	v_bitop3_b32 v90, v226, s19, v90 bitop3:0x36
	v_add_f32_e32 v228, v228, v229
	v_cmp_gt_i32_e64 s[4:5], 0, v228
	v_not_b32_e32 v229, v228
	v_or_b32_e32 v238, 0x80000000, v228
	v_cndmask_b32_e64 v228, v238, v229, s[4:5]
	v_and_b32_e32 v228, 0xffffff00, v228
	v_bitop3_b32 v89, v228, s19, v89 bitop3:0x36
	v_add_f32_e32 v230, v230, v231
	v_cmp_gt_i32_e64 s[4:5], 0, v230
	v_not_b32_e32 v231, v230
	v_or_b32_e32 v238, 0x80000000, v230
	v_cndmask_b32_e64 v230, v238, v231, s[4:5]
	v_and_b32_e32 v230, 0xffffff00, v230
	v_bitop3_b32 v92, v230, s19, v92 bitop3:0x36
	v_add_f32_e32 v232, v232, v233
	v_cmp_gt_i32_e64 s[4:5], 0, v232
	v_not_b32_e32 v233, v232
	v_or_b32_e32 v238, 0x80000000, v232
	v_cndmask_b32_e64 v232, v238, v233, s[4:5]
	v_and_b32_e32 v232, 0xffffff00, v232
	v_bitop3_b32 v91, v232, s19, v91 bitop3:0x36
	v_add_f32_e32 v234, v234, v235
	v_cmp_gt_i32_e64 s[4:5], 0, v234
	v_not_b32_e32 v235, v234
	v_or_b32_e32 v238, 0x80000000, v234
	v_cndmask_b32_e64 v234, v238, v235, s[4:5]
	v_and_b32_e32 v234, 0xffffff00, v234
	v_bitop3_b32 v94, v234, s19, v94 bitop3:0x36
	v_add_f32_e32 v236, v236, v237
	v_cmp_gt_i32_e64 s[4:5], 0, v236
	v_not_b32_e32 v237, v236
	v_or_b32_e32 v238, 0x80000000, v236
	v_cndmask_b32_e64 v236, v238, v237, s[4:5]
	v_and_b32_e32 v236, 0xffffff00, v236
	v_bitop3_b32 v93, v236, s19, v70 bitop3:0x36
	s_or_b64 exec, exec, s[6:7]
	s_mov_b64 s[4:5], exec
	s_branch .LBB0_1650
